# stream: static priority raise (s_setprio 3) for the four waves that sum the partial u vectors, dropped after their LDS publish; rest as v40
# baseline (speedup 1.0000x reference)
_Z13stream_kernelPKfPf:
	s_load_dwordx4 s[4:7], s[0:1], 0x0
	s_movk_i32 s0, 0x100
	v_readfirstlane_b32 s3, v0
	v_cmp_gt_u32_e32 vcc, s0, v0
	s_and_saveexec_b64 s[0:1], vcc
	s_cbranch_execz .LBB1_2
	s_setprio 3
	v_lshlrev_b32_e32 v18, 4, v0
	v_mov_b32_e32 v19, 0
	s_waitcnt lgkmcnt(0)
	v_lshl_add_u64 v[14:15], s[6:7], 0, v[18:19]
	v_add_co_u32_e32 v16, vcc, 0x1000, v14
	global_load_dwordx4 v[2:5], v18, s[6:7]
	s_nop 0
	v_addc_co_u32_e32 v17, vcc, 0, v15, vcc
	v_add_co_u32_e32 v20, vcc, 0x2000, v14
	s_nop 1
	v_addc_co_u32_e32 v21, vcc, 0, v15, vcc
	v_add_co_u32_e32 v14, vcc, 0x3000, v14
	global_load_dwordx4 v[6:9], v[16:17], off
	global_load_dwordx4 v[10:13], v[20:21], off
	v_addc_co_u32_e32 v15, vcc, 0, v15, vcc
	global_load_dwordx4 v[14:17], v[14:15], off
	s_waitcnt vmcnt(2)
	v_pk_add_f32 v[4:5], v[4:5], v[8:9]
	v_pk_add_f32 v[2:3], v[2:3], v[6:7]
	s_waitcnt vmcnt(1)
	v_pk_add_f32 v[4:5], v[4:5], v[12:13]
	v_pk_add_f32 v[2:3], v[2:3], v[10:11]
	s_waitcnt vmcnt(0)
	v_pk_add_f32 v[4:5], v[4:5], v[16:17]
	v_pk_add_f32 v[2:3], v[2:3], v[14:15]
	ds_write_b128 v18, v[2:5]
	s_setprio 0
